# gate path: log-sigmoid via v_log_f32 instead of library log1pf
# speedup vs baseline: 1.0113x; 1.0113x over previous
.LBB0_146:
	s_or_b64 exec, exec, s[72:73]
	v_lshl_add_u64 v[70:71], v[78:79], 0, s[66:67]
	s_waitcnt lgkmcnt(0)
	v_mfma_f32_16x16x32_bf16 v[78:81], v[6:9], v[66:69], 0
	s_add_i32 s70, s96, s70
	s_cmpk_lt_i32 s70, 0x100
	v_lshl_add_u64 v[76:77], v[76:77], 0, s[24:25]
	s_nop 4
	v_add_f32_e32 v78, v10, v78
	v_mul_f32_e64 v82, |v78|, s35
	v_exp_f32_e32 v89, v82
	v_add_f32_e32 v83, v11, v79
	v_min_f32_e32 v82, 0, v78
	v_mul_f32_e64 v78, |v83|, s35
	v_exp_f32_e32 v116, v78
	v_add_f32_e32 v80, v12, v80
	v_min_f32_e32 v83, 0, v83
	v_add_f32_e32 v81, v13, v81
	v_mul_f32_e64 v92, |v80|, s35
	v_exp_f32_e32 v118, v92
	v_min_f32_e32 v80, 0, v80
	v_add_f32_e32 v91, 1.0, v116
	v_log_f32_e32 v91, v91
	s_nop 0
	v_mul_f32_e32 v91, 0x3f317218, v91
	v_add_f32_e32 v90, 1.0, v89
	v_log_f32_e32 v90, v90
	s_nop 0
	v_mul_f32_e32 v90, 0x3f317218, v90
	v_pk_add_f32 v[90:91], v[82:83], v[90:91] neg_lo:[0,1] neg_hi:[0,1]
	v_mul_f32_e64 v82, |v81|, s35
	v_exp_f32_e32 v119, v82
	v_min_f32_e32 v81, 0, v81
	v_lshl_add_u64 v[94:95], s[2:3], 2, v[70:71]
	v_add_f32_e32 v83, 1.0, v119
	v_log_f32_e32 v83, v83
	s_nop 0
	v_mul_f32_e32 v83, 0x3f317218, v83
	v_add_f32_e32 v82, 1.0, v118
	v_log_f32_e32 v82, v82
	s_nop 0
	v_mul_f32_e32 v82, 0x3f317218, v82
	v_pk_add_f32 v[80:81], v[80:81], v[82:83] neg_lo:[0,1] neg_hi:[0,1]
	s_nop 0
	v_pk_mul_f32 v[82:83], v[80:81], s[44:45] op_sel_hi:[1,0]
	v_pk_mul_f32 v[80:81], v[90:91], s[44:45] op_sel_hi:[1,0]
	v_mfma_f32_16x16x32_bf16 v[90:93], v[2:5], v[66:69], 0
	global_store_dwordx4 v[94:95], v[80:83], off
	s_nop 6
	v_add_f32_e32 v89, v14, v90
	v_mul_f32_e64 v90, |v89|, s35
	v_exp_f32_e32 v118, v90
	v_min_f32_e32 v80, 0, v89
	v_add_f32_e32 v81, v15, v91
	v_mul_f32_e64 v82, |v81|, s35
	v_exp_f32_e32 v119, v82
	v_min_f32_e32 v81, 0, v81
	v_add_f32_e32 v89, v16, v92
	v_mul_f32_e64 v90, |v89|, s35
	v_add_f32_e32 v83, 1.0, v119
	v_log_f32_e32 v83, v83
	s_nop 0
	v_mul_f32_e32 v83, 0x3f317218, v83
	v_exp_f32_e32 v119, v90
	v_add_f32_e32 v82, 1.0, v118
	v_log_f32_e32 v82, v82
	s_nop 0
	v_mul_f32_e32 v82, 0x3f317218, v82
	v_pk_add_f32 v[80:81], v[80:81], v[82:83] neg_lo:[0,1] neg_hi:[0,1]
	v_min_f32_e32 v82, 0, v89
	v_add_f32_e32 v83, v17, v93
	v_mul_f32_e64 v90, |v83|, s35
	v_exp_f32_e32 v118, v90
	v_min_f32_e32 v83, 0, v83
	v_pk_mul_f32 v[80:81], v[80:81], s[44:45] op_sel_hi:[1,0]
	v_lshl_add_u64 v[94:95], s[10:11], 2, v[70:71]
	v_add_f32_e32 v91, 1.0, v118
	v_log_f32_e32 v91, v91
	s_nop 0
	v_mul_f32_e32 v91, 0x3f317218, v91
	v_add_f32_e32 v90, 1.0, v119
	v_log_f32_e32 v90, v90
	s_nop 0
	v_mul_f32_e32 v90, 0x3f317218, v90
	v_pk_add_f32 v[82:83], v[82:83], v[90:91] neg_lo:[0,1] neg_hi:[0,1]
	v_mfma_f32_16x16x32_bf16 v[90:93], v[22:25], v[66:69], 0
	v_mul_f32_e64 v82, v82, s44
	v_mul_f32_e64 v83, v83, s44
	global_store_dwordx4 v[94:95], v[80:83], off
	s_nop 4
	v_add_f32_e32 v89, v26, v90
	v_mul_f32_e64 v90, |v89|, s35
	v_exp_f32_e32 v118, v90
	v_min_f32_e32 v80, 0, v89
	v_add_f32_e32 v81, v27, v91
	v_mul_f32_e64 v82, |v81|, s35
	v_exp_f32_e32 v119, v82
	v_min_f32_e32 v81, 0, v81
	v_add_f32_e32 v89, v28, v92
	v_mul_f32_e64 v90, |v89|, s35
	v_add_f32_e32 v83, 1.0, v119
	v_log_f32_e32 v83, v83
	s_nop 0
	v_mul_f32_e32 v83, 0x3f317218, v83
	v_exp_f32_e32 v119, v90
	v_add_f32_e32 v82, 1.0, v118
	v_log_f32_e32 v82, v82
	s_nop 0
	v_mul_f32_e32 v82, 0x3f317218, v82
	v_pk_add_f32 v[80:81], v[80:81], v[82:83] neg_lo:[0,1] neg_hi:[0,1]
	v_min_f32_e32 v82, 0, v89
	v_add_f32_e32 v83, v29, v93
	v_mul_f32_e64 v90, |v83|, s35
	v_exp_f32_e32 v118, v90
	v_min_f32_e32 v83, 0, v83
	v_pk_mul_f32 v[80:81], v[80:81], s[44:45] op_sel_hi:[1,0]
	v_lshl_add_u64 v[94:95], s[12:13], 2, v[70:71]
	v_add_f32_e32 v91, 1.0, v118
	v_log_f32_e32 v91, v91
	s_nop 0
	v_mul_f32_e32 v91, 0x3f317218, v91
	v_add_f32_e32 v90, 1.0, v119
	v_log_f32_e32 v90, v90
	s_nop 0
	v_mul_f32_e32 v90, 0x3f317218, v90
	v_pk_add_f32 v[82:83], v[82:83], v[90:91] neg_lo:[0,1] neg_hi:[0,1]
	v_mfma_f32_16x16x32_bf16 v[90:93], v[18:21], v[66:69], 0
	v_mul_f32_e64 v82, v82, s44
	v_mul_f32_e64 v83, v83, s44
	global_store_dwordx4 v[94:95], v[80:83], off
	s_nop 4
	v_add_f32_e32 v89, v30, v90
	v_mul_f32_e64 v90, |v89|, s35
	v_exp_f32_e32 v118, v90
	v_min_f32_e32 v80, 0, v89
	v_add_f32_e32 v81, v31, v91
	v_mul_f32_e64 v82, |v81|, s35
	v_exp_f32_e32 v119, v82
	v_min_f32_e32 v81, 0, v81
	v_add_f32_e32 v89, v32, v92
	v_mul_f32_e64 v90, |v89|, s35
	v_add_f32_e32 v83, 1.0, v119
	v_log_f32_e32 v83, v83
	s_nop 0
	v_mul_f32_e32 v83, 0x3f317218, v83
	v_exp_f32_e32 v119, v90
	v_add_f32_e32 v82, 1.0, v118
	v_log_f32_e32 v82, v82
	s_nop 0
	v_mul_f32_e32 v82, 0x3f317218, v82
	v_pk_add_f32 v[80:81], v[80:81], v[82:83] neg_lo:[0,1] neg_hi:[0,1]
	v_min_f32_e32 v82, 0, v89
	v_add_f32_e32 v83, v33, v93
	v_mul_f32_e64 v90, |v83|, s35
	v_exp_f32_e32 v118, v90
	v_min_f32_e32 v83, 0, v83
	v_pk_mul_f32 v[80:81], v[80:81], s[44:45] op_sel_hi:[1,0]
	v_lshl_add_u64 v[94:95], s[14:15], 2, v[70:71]
	v_add_f32_e32 v91, 1.0, v118
	v_log_f32_e32 v91, v91
	s_nop 0
	v_mul_f32_e32 v91, 0x3f317218, v91
	v_add_f32_e32 v90, 1.0, v119
	v_log_f32_e32 v90, v90
	s_nop 0
	v_mul_f32_e32 v90, 0x3f317218, v90
	v_pk_add_f32 v[82:83], v[82:83], v[90:91] neg_lo:[0,1] neg_hi:[0,1]
	v_mfma_f32_16x16x32_bf16 v[90:93], v[38:41], v[66:69], 0
	v_mul_f32_e64 v82, v82, s44
	v_mul_f32_e64 v83, v83, s44
	global_store_dwordx4 v[94:95], v[80:83], off
	s_nop 4
	v_add_f32_e32 v89, v42, v90
	v_mul_f32_e64 v90, |v89|, s35
	v_exp_f32_e32 v118, v90
	v_min_f32_e32 v80, 0, v89
	v_add_f32_e32 v81, v43, v91
	v_mul_f32_e64 v82, |v81|, s35
	v_exp_f32_e32 v119, v82
	v_min_f32_e32 v81, 0, v81
	v_add_f32_e32 v89, v44, v92
	v_mul_f32_e64 v90, |v89|, s35
	v_add_f32_e32 v83, 1.0, v119
	v_log_f32_e32 v83, v83
	s_nop 0
	v_mul_f32_e32 v83, 0x3f317218, v83
	v_exp_f32_e32 v119, v90
	v_add_f32_e32 v82, 1.0, v118
	v_log_f32_e32 v82, v82
	s_nop 0
	v_mul_f32_e32 v82, 0x3f317218, v82
	v_pk_add_f32 v[80:81], v[80:81], v[82:83] neg_lo:[0,1] neg_hi:[0,1]
	v_min_f32_e32 v82, 0, v89
	v_add_f32_e32 v83, v45, v93
	v_mul_f32_e64 v90, |v83|, s35
	v_exp_f32_e32 v118, v90
	v_min_f32_e32 v83, 0, v83
	v_pk_mul_f32 v[80:81], v[80:81], s[44:45] op_sel_hi:[1,0]
	v_lshl_add_u64 v[94:95], s[16:17], 2, v[70:71]
	v_add_f32_e32 v91, 1.0, v118
	v_log_f32_e32 v91, v91
	s_nop 0
	v_mul_f32_e32 v91, 0x3f317218, v91
	v_add_f32_e32 v90, 1.0, v119
	v_log_f32_e32 v90, v90
	s_nop 0
	v_mul_f32_e32 v90, 0x3f317218, v90
	v_pk_add_f32 v[82:83], v[82:83], v[90:91] neg_lo:[0,1] neg_hi:[0,1]
	v_mfma_f32_16x16x32_bf16 v[90:93], v[34:37], v[66:69], 0
	v_mul_f32_e64 v82, v82, s44
	v_mul_f32_e64 v83, v83, s44
	global_store_dwordx4 v[94:95], v[80:83], off
	s_nop 4
	v_add_f32_e32 v89, v46, v90
	v_mul_f32_e64 v90, |v89|, s35
	v_exp_f32_e32 v118, v90
	v_min_f32_e32 v80, 0, v89
	v_add_f32_e32 v81, v47, v91
	v_mul_f32_e64 v82, |v81|, s35
	v_exp_f32_e32 v119, v82
	v_min_f32_e32 v81, 0, v81
	v_add_f32_e32 v89, v48, v92
	v_mul_f32_e64 v90, |v89|, s35
	v_add_f32_e32 v83, 1.0, v119
	v_log_f32_e32 v83, v83
	s_nop 0
	v_mul_f32_e32 v83, 0x3f317218, v83
	v_exp_f32_e32 v119, v90
	v_add_f32_e32 v82, 1.0, v118
	v_log_f32_e32 v82, v82
	s_nop 0
	v_mul_f32_e32 v82, 0x3f317218, v82
	v_pk_add_f32 v[80:81], v[80:81], v[82:83] neg_lo:[0,1] neg_hi:[0,1]
	v_min_f32_e32 v82, 0, v89
	v_add_f32_e32 v83, v49, v93
	v_mul_f32_e64 v90, |v83|, s35
	v_exp_f32_e32 v118, v90
	v_min_f32_e32 v83, 0, v83
	v_pk_mul_f32 v[80:81], v[80:81], s[44:45] op_sel_hi:[1,0]
	v_lshl_add_u64 v[94:95], s[18:19], 2, v[70:71]
	v_add_f32_e32 v91, 1.0, v118
	v_log_f32_e32 v91, v91
	s_nop 0
	v_mul_f32_e32 v91, 0x3f317218, v91
	v_add_f32_e32 v90, 1.0, v119
	v_log_f32_e32 v90, v90
	s_nop 0
	v_mul_f32_e32 v90, 0x3f317218, v90
	v_pk_add_f32 v[82:83], v[82:83], v[90:91] neg_lo:[0,1] neg_hi:[0,1]
	v_mfma_f32_16x16x32_bf16 v[90:93], v[54:57], v[66:69], 0
	v_mul_f32_e64 v82, v82, s44
	v_mul_f32_e64 v83, v83, s44
	global_store_dwordx4 v[94:95], v[80:83], off
	v_mfma_f32_16x16x32_bf16 v[66:69], v[50:53], v[66:69], 0
	s_nop 3
	v_add_f32_e32 v89, v58, v90
	v_mul_f32_e64 v90, |v89|, s35
	v_exp_f32_e32 v118, v90
	v_min_f32_e32 v80, 0, v89
	v_add_f32_e32 v66, v62, v66
	v_add_f32_e32 v67, v63, v67
	v_add_f32_e32 v81, v59, v91
	v_mul_f32_e64 v82, |v81|, s35
	v_exp_f32_e32 v119, v82
	v_min_f32_e32 v81, 0, v81
	v_add_f32_e32 v68, v64, v68
	v_add_f32_e32 v69, v65, v69
	v_add_f32_e32 v89, v60, v92
	v_mul_f32_e64 v90, |v89|, s35
	v_add_f32_e32 v83, 1.0, v119
	v_log_f32_e32 v83, v83
	s_nop 0
	v_mul_f32_e32 v83, 0x3f317218, v83
	v_exp_f32_e32 v119, v90
	v_add_f32_e32 v82, 1.0, v118
	v_log_f32_e32 v82, v82
	s_nop 0
	v_mul_f32_e32 v82, 0x3f317218, v82
	v_pk_add_f32 v[80:81], v[80:81], v[82:83] neg_lo:[0,1] neg_hi:[0,1]
	v_min_f32_e32 v82, 0, v89
	v_add_f32_e32 v83, v61, v93
	v_mul_f32_e64 v90, |v83|, s35
	v_exp_f32_e32 v118, v90
	v_min_f32_e32 v83, 0, v83
	v_pk_mul_f32 v[80:81], v[80:81], s[44:45] op_sel_hi:[1,0]
	v_add_f32_e32 v91, 1.0, v118
	v_log_f32_e32 v91, v91
	s_nop 0
	v_mul_f32_e32 v91, 0x3f317218, v91
	v_add_f32_e32 v90, 1.0, v119
	v_log_f32_e32 v90, v90
	s_nop 0
	v_mul_f32_e32 v90, 0x3f317218, v90
	v_mul_f32_e64 v89, |v66|, s35
	v_exp_f32_e32 v89, v89
	v_pk_add_f32 v[82:83], v[82:83], v[90:91] neg_lo:[0,1] neg_hi:[0,1]
	v_lshl_add_u64 v[90:91], s[20:21], 2, v[70:71]
	v_pk_mul_f32 v[82:83], v[82:83], s[44:45] op_sel_hi:[1,0]
	global_store_dwordx4 v[90:91], v[80:83], off
	v_min_f32_e32 v66, 0, v66
	v_lshl_add_u64 v[70:71], s[22:23], 2, v[70:71]
	v_mul_f32_e64 v80, |v67|, s35
	v_exp_f32_e32 v114, v80
	v_min_f32_e32 v67, 0, v67
	v_mul_f32_e64 v82, |v68|, s35
	v_min_f32_e32 v68, 0, v68
	v_add_f32_e32 v81, 1.0, v114
	v_log_f32_e32 v81, v81
	s_nop 0
	v_mul_f32_e32 v81, 0x3f317218, v81
	v_exp_f32_e32 v114, v82
	v_add_f32_e32 v80, 1.0, v89
	v_log_f32_e32 v80, v80
	s_nop 0
	v_mul_f32_e32 v80, 0x3f317218, v80
	v_pk_add_f32 v[66:67], v[66:67], v[80:81] neg_lo:[0,1] neg_hi:[0,1]
	v_mul_f32_e64 v80, |v69|, s35
	v_exp_f32_e32 v115, v80
	v_min_f32_e32 v69, 0, v69
	v_pk_mul_f32 v[66:67], v[66:67], s[44:45] op_sel_hi:[1,0]
	v_add_f32_e32 v79, 1.0, v115
	v_log_f32_e32 v79, v79
	s_nop 0
	v_mul_f32_e32 v79, 0x3f317218, v79
	v_cmp_lt_f32_e64 vcc, |v114|, s45
	v_add_f32_e32 v78, 1.0, v114
	v_log_f32_e32 v78, v78
	s_nop 0
	v_mul_f32_e32 v78, 0x3f317218, v78
	v_pk_add_f32 v[68:69], v[68:69], v[78:79] neg_lo:[0,1] neg_hi:[0,1]
	s_nop 0
	v_pk_mul_f32 v[68:69], v[68:69], s[44:45] op_sel_hi:[1,0]
	global_store_dwordx4 v[70:71], v[66:69], off
	s_barrier
	s_cbranch_scc0 .LBB0_161

.LBB0_153:
	s_nop 0
	v_mov_b32_e32 v66, 0
	v_mov_b32_e32 v68, 0
	v_mov_b32_e32 v69, 0
	v_mov_b32_e32 v70, 0
	v_mov_b32_e32 v71, 0
	s_waitcnt lgkmcnt(0)
	s_barrier
	s_and_saveexec_b64 s[72:73], s[4:5]
	ds_read_b128 v[68:71], v72
	s_or_b64 exec, exec, s[72:73]
	s_waitcnt lgkmcnt(0)
	v_mfma_f32_16x16x32_bf16 v[80:83], v[6:9], v[68:71], 0
	s_ashr_i32 s71, s70, 31
	s_lshl_b64 s[72:73], s[70:71], 18
	v_lshl_or_b32 v78, v130, 12, s72
	s_nop 4
	v_add_f32_e32 v67, v10, v80
	v_mul_f32_e64 v79, |v67|, s35
	v_exp_f32_e32 v89, v79
	v_min_f32_e32 v90, 0, v67
	v_add_f32_e32 v82, v12, v82
	v_add_f32_e32 v83, v13, v83
	v_add_f32_e32 v91, v11, v81
	v_mul_f32_e64 v80, |v91|, s35
	v_exp_f32_e32 v118, v80
	v_min_f32_e32 v91, 0, v91
	v_mov_b32_e32 v79, s73
	v_lshl_add_u64 v[78:79], v[74:75], 0, v[78:79]
	v_add_f32_e32 v93, 1.0, v118
	v_log_f32_e32 v93, v93
	s_nop 0
	v_mul_f32_e32 v93, 0x3f317218, v93
	v_mul_f32_e64 v92, |v82|, s35
	v_exp_f32_e32 v120, v92
	v_min_f32_e32 v82, 0, v82
	v_add_f32_e32 v92, 1.0, v89
	v_log_f32_e32 v92, v92
	s_nop 0
	v_mul_f32_e32 v92, 0x3f317218, v92
	v_pk_add_f32 v[90:91], v[90:91], v[92:93] neg_lo:[0,1] neg_hi:[0,1]
	v_mul_f32_e64 v92, |v83|, s35
	v_exp_f32_e32 v121, v92
	v_min_f32_e32 v83, 0, v83
	v_pk_mul_f32 v[90:91], v[90:91], s[44:45] op_sel_hi:[1,0]
	v_mfma_f32_16x16x32_bf16 v[94:97], v[2:5], v[68:71], 0
	v_add_f32_e32 v93, 1.0, v121
	v_log_f32_e32 v93, v93
	s_nop 0
	v_mul_f32_e32 v93, 0x3f317218, v93
	v_add_f32_e32 v92, 1.0, v120
	v_log_f32_e32 v92, v92
	s_nop 0
	v_mul_f32_e32 v92, 0x3f317218, v92
	v_pk_add_f32 v[82:83], v[82:83], v[92:93] neg_lo:[0,1] neg_hi:[0,1]
	v_add_f32_e32 v67, v14, v94
	v_pk_mul_f32 v[92:93], v[82:83], s[44:45] op_sel_hi:[1,0]
	v_mul_f32_e64 v82, |v67|, s35
	v_exp_f32_e32 v89, v82
	v_lshl_add_u64 v[82:83], s[2:3], 2, v[78:79]
	global_store_dwordx4 v[82:83], v[90:93], off
	s_nop 1
	v_min_f32_e32 v90, 0, v67
	v_add_f32_e32 v91, v15, v95
	v_mul_f32_e64 v92, |v91|, s35
	v_exp_f32_e32 v122, v92
	v_min_f32_e32 v91, 0, v91
	v_add_f32_e32 v94, v16, v96
	v_add_f32_e32 v93, 1.0, v122
	v_log_f32_e32 v93, v93
	s_nop 0
	v_mul_f32_e32 v93, 0x3f317218, v93
	v_mul_f32_e64 v92, |v94|, s35
	v_exp_f32_e32 v122, v92
	v_add_f32_e32 v92, 1.0, v89
	v_log_f32_e32 v92, v92
	s_nop 0
	v_mul_f32_e32 v92, 0x3f317218, v92
	v_pk_add_f32 v[90:91], v[90:91], v[92:93] neg_lo:[0,1] neg_hi:[0,1]
	v_add_f32_e32 v93, v17, v97
	v_min_f32_e32 v92, 0, v94
	v_mul_f32_e64 v94, |v93|, s35
	v_exp_f32_e32 v123, v94
	v_min_f32_e32 v93, 0, v93
	v_pk_mul_f32 v[90:91], v[90:91], s[44:45] op_sel_hi:[1,0]
	v_add_f32_e32 v95, 1.0, v123
	v_log_f32_e32 v95, v95
	s_nop 0
	v_mul_f32_e32 v95, 0x3f317218, v95
	v_add_f32_e32 v94, 1.0, v122
	v_log_f32_e32 v94, v94
	s_nop 0
	v_mul_f32_e32 v94, 0x3f317218, v94
	v_pk_add_f32 v[92:93], v[92:93], v[94:95] neg_lo:[0,1] neg_hi:[0,1]
	v_mfma_f32_16x16x32_bf16 v[94:97], v[22:25], v[68:71], 0
	v_mul_f32_e64 v92, v92, s44
	v_mul_f32_e64 v93, v93, s44
	global_store_dwordx4 v[82:83], v[90:93], off offset:64
	s_nop 4
	v_add_f32_e32 v67, v26, v94
	v_mul_f32_e64 v89, |v67|, s35
	v_exp_f32_e32 v89, v89
	v_min_f32_e32 v90, 0, v67
	v_add_f32_e32 v91, v27, v95
	v_mul_f32_e64 v92, |v91|, s35
	v_exp_f32_e32 v122, v92
	v_min_f32_e32 v91, 0, v91
	v_add_f32_e32 v94, v28, v96
	v_add_f32_e32 v93, 1.0, v122
	v_log_f32_e32 v93, v93
	s_nop 0
	v_mul_f32_e32 v93, 0x3f317218, v93
	v_mul_f32_e64 v92, |v94|, s35
	v_exp_f32_e32 v122, v92
	v_add_f32_e32 v92, 1.0, v89
	v_log_f32_e32 v92, v92
	s_nop 0
	v_mul_f32_e32 v92, 0x3f317218, v92
	v_pk_add_f32 v[90:91], v[90:91], v[92:93] neg_lo:[0,1] neg_hi:[0,1]
	v_add_f32_e32 v93, v29, v97
	v_min_f32_e32 v92, 0, v94
	v_mul_f32_e64 v94, |v93|, s35
	v_exp_f32_e32 v123, v94
	v_min_f32_e32 v93, 0, v93
	v_pk_mul_f32 v[90:91], v[90:91], s[44:45] op_sel_hi:[1,0]
	v_add_f32_e32 v95, 1.0, v123
	v_log_f32_e32 v95, v95
	s_nop 0
	v_mul_f32_e32 v95, 0x3f317218, v95
	v_add_f32_e32 v94, 1.0, v122
	v_log_f32_e32 v94, v94
	s_nop 0
	v_mul_f32_e32 v94, 0x3f317218, v94
	v_pk_add_f32 v[92:93], v[92:93], v[94:95] neg_lo:[0,1] neg_hi:[0,1]
	v_mfma_f32_16x16x32_bf16 v[94:97], v[18:21], v[68:71], 0
	v_mul_f32_e64 v92, v92, s44
	v_mul_f32_e64 v93, v93, s44
	global_store_dwordx4 v[82:83], v[90:93], off offset:128
	s_nop 4
	v_add_f32_e32 v67, v30, v94
	v_mul_f32_e64 v89, |v67|, s35
	v_exp_f32_e32 v89, v89
	v_min_f32_e32 v90, 0, v67
	v_add_f32_e32 v91, v31, v95
	v_mul_f32_e64 v92, |v91|, s35
	v_exp_f32_e32 v122, v92
	v_min_f32_e32 v91, 0, v91
	v_add_f32_e32 v94, v32, v96
	v_add_f32_e32 v93, 1.0, v122
	v_log_f32_e32 v93, v93
	s_nop 0
	v_mul_f32_e32 v93, 0x3f317218, v93
	v_mul_f32_e64 v92, |v94|, s35
	v_exp_f32_e32 v122, v92
	v_add_f32_e32 v92, 1.0, v89
	v_log_f32_e32 v92, v92
	s_nop 0
	v_mul_f32_e32 v92, 0x3f317218, v92
	v_pk_add_f32 v[90:91], v[90:91], v[92:93] neg_lo:[0,1] neg_hi:[0,1]
	v_add_f32_e32 v93, v33, v97
	v_min_f32_e32 v92, 0, v94
	v_mul_f32_e64 v94, |v93|, s35
	v_exp_f32_e32 v123, v94
	v_min_f32_e32 v93, 0, v93
	v_pk_mul_f32 v[90:91], v[90:91], s[44:45] op_sel_hi:[1,0]
	v_add_f32_e32 v95, 1.0, v123
	v_log_f32_e32 v95, v95
	s_nop 0
	v_mul_f32_e32 v95, 0x3f317218, v95
	v_add_f32_e32 v94, 1.0, v122
	v_log_f32_e32 v94, v94
	s_nop 0
	v_mul_f32_e32 v94, 0x3f317218, v94
	v_pk_add_f32 v[92:93], v[92:93], v[94:95] neg_lo:[0,1] neg_hi:[0,1]
	v_mfma_f32_16x16x32_bf16 v[94:97], v[38:41], v[68:71], 0
	v_mul_f32_e64 v92, v92, s44
	v_mul_f32_e64 v93, v93, s44
	global_store_dwordx4 v[82:83], v[90:93], off offset:192
	s_nop 4
	v_add_f32_e32 v67, v42, v94
	v_mul_f32_e64 v89, |v67|, s35
	v_exp_f32_e32 v89, v89
	v_min_f32_e32 v90, 0, v67
	v_add_f32_e32 v91, v43, v95
	v_mul_f32_e64 v92, |v91|, s35
	v_exp_f32_e32 v122, v92
	v_min_f32_e32 v91, 0, v91
	v_add_f32_e32 v94, v44, v96
	v_add_f32_e32 v93, 1.0, v122
	v_log_f32_e32 v93, v93
	s_nop 0
	v_mul_f32_e32 v93, 0x3f317218, v93
	v_mul_f32_e64 v92, |v94|, s35
	v_exp_f32_e32 v122, v92
	v_add_f32_e32 v92, 1.0, v89
	v_log_f32_e32 v92, v92
	s_nop 0
	v_mul_f32_e32 v92, 0x3f317218, v92
	v_pk_add_f32 v[90:91], v[90:91], v[92:93] neg_lo:[0,1] neg_hi:[0,1]
	v_add_f32_e32 v93, v45, v97
	v_min_f32_e32 v92, 0, v94
	v_mul_f32_e64 v94, |v93|, s35
	v_exp_f32_e32 v123, v94
	v_min_f32_e32 v93, 0, v93
	v_pk_mul_f32 v[90:91], v[90:91], s[44:45] op_sel_hi:[1,0]
	v_add_f32_e32 v95, 1.0, v123
	v_log_f32_e32 v95, v95
	s_nop 0
	v_mul_f32_e32 v95, 0x3f317218, v95
	v_add_f32_e32 v94, 1.0, v122
	v_log_f32_e32 v94, v94
	s_nop 0
	v_mul_f32_e32 v94, 0x3f317218, v94
	v_pk_add_f32 v[92:93], v[92:93], v[94:95] neg_lo:[0,1] neg_hi:[0,1]
	v_mfma_f32_16x16x32_bf16 v[94:97], v[34:37], v[68:71], 0
	v_mul_f32_e64 v92, v92, s44
	v_mul_f32_e64 v93, v93, s44
	global_store_dwordx4 v[82:83], v[90:93], off offset:256
	s_nop 4
	v_add_f32_e32 v67, v46, v94
	v_mul_f32_e64 v89, |v67|, s35
	v_exp_f32_e32 v89, v89
	v_min_f32_e32 v90, 0, v67
	v_add_f32_e32 v91, v47, v95
	v_mul_f32_e64 v92, |v91|, s35
	v_exp_f32_e32 v122, v92
	v_min_f32_e32 v91, 0, v91
	v_add_f32_e32 v94, v48, v96
	v_add_f32_e32 v93, 1.0, v122
	v_log_f32_e32 v93, v93
	s_nop 0
	v_mul_f32_e32 v93, 0x3f317218, v93
	v_mul_f32_e64 v92, |v94|, s35
	v_exp_f32_e32 v122, v92
	v_add_f32_e32 v92, 1.0, v89
	v_log_f32_e32 v92, v92
	s_nop 0
	v_mul_f32_e32 v92, 0x3f317218, v92
	v_pk_add_f32 v[90:91], v[90:91], v[92:93] neg_lo:[0,1] neg_hi:[0,1]
	v_add_f32_e32 v93, v49, v97
	v_min_f32_e32 v92, 0, v94
	v_mul_f32_e64 v94, |v93|, s35
	v_exp_f32_e32 v123, v94
	v_min_f32_e32 v93, 0, v93
	v_pk_mul_f32 v[90:91], v[90:91], s[44:45] op_sel_hi:[1,0]
	v_add_f32_e32 v95, 1.0, v123
	v_log_f32_e32 v95, v95
	s_nop 0
	v_mul_f32_e32 v95, 0x3f317218, v95
	v_add_f32_e32 v94, 1.0, v122
	v_log_f32_e32 v94, v94
	s_nop 0
	v_mul_f32_e32 v94, 0x3f317218, v94
	v_pk_add_f32 v[92:93], v[92:93], v[94:95] neg_lo:[0,1] neg_hi:[0,1]
	v_mfma_f32_16x16x32_bf16 v[94:97], v[54:57], v[68:71], 0
	v_mul_f32_e64 v92, v92, s44
	v_mul_f32_e64 v93, v93, s44
	global_store_dwordx4 v[82:83], v[90:93], off offset:320
	v_mfma_f32_16x16x32_bf16 v[68:71], v[50:53], v[68:71], 0
	s_nop 3
	v_add_f32_e32 v67, v58, v94
	v_mul_f32_e64 v89, |v67|, s35
	v_exp_f32_e32 v89, v89
	v_min_f32_e32 v90, 0, v67
	v_add_f32_e32 v69, v63, v69
	v_add_f32_e32 v70, v64, v70
	v_add_f32_e32 v91, v59, v95
	v_mul_f32_e64 v92, |v91|, s35
	v_exp_f32_e32 v122, v92
	v_min_f32_e32 v91, 0, v91
	v_add_f32_e32 v71, v65, v71
	v_add_f32_e32 v94, v60, v96
	v_add_f32_e32 v93, 1.0, v122
	v_log_f32_e32 v93, v93
	s_nop 0
	v_mul_f32_e32 v93, 0x3f317218, v93
	v_mul_f32_e64 v92, |v94|, s35
	v_exp_f32_e32 v122, v92
	v_add_f32_e32 v92, 1.0, v89
	v_log_f32_e32 v92, v92
	s_nop 0
	v_mul_f32_e32 v92, 0x3f317218, v92
	v_pk_add_f32 v[90:91], v[90:91], v[92:93] neg_lo:[0,1] neg_hi:[0,1]
	v_add_f32_e32 v93, v61, v97
	v_min_f32_e32 v92, 0, v94
	v_mul_f32_e64 v94, |v93|, s35
	v_exp_f32_e32 v123, v94
	v_min_f32_e32 v93, 0, v93
	v_pk_mul_f32 v[90:91], v[90:91], s[44:45] op_sel_hi:[1,0]
	v_add_f32_e32 v95, 1.0, v123
	v_log_f32_e32 v95, v95
	s_nop 0
	v_mul_f32_e32 v95, 0x3f317218, v95
	v_add_f32_e32 v94, 1.0, v122
	v_log_f32_e32 v94, v94
	s_nop 0
	v_mul_f32_e32 v94, 0x3f317218, v94
	v_add_f32_e32 v67, v62, v68
	v_mul_f32_e64 v68, |v67|, s35
	v_exp_f32_e32 v89, v68
	v_pk_add_f32 v[92:93], v[92:93], v[94:95] neg_lo:[0,1] neg_hi:[0,1]
	v_min_f32_e32 v68, 0, v67
	v_pk_mul_f32 v[92:93], v[92:93], s[44:45] op_sel_hi:[1,0]
	global_store_dwordx4 v[82:83], v[90:93], off offset:384
	s_nop 1
	v_mul_f32_e64 v90, |v69|, s35
	v_exp_f32_e32 v118, v90
	v_min_f32_e32 v69, 0, v69
	v_add_f32_e32 v91, 1.0, v118
	v_log_f32_e32 v91, v91
	s_nop 0
	v_mul_f32_e32 v91, 0x3f317218, v91
	v_mul_f32_e64 v90, |v70|, s35
	v_exp_f32_e32 v118, v90
	v_min_f32_e32 v70, 0, v70
	v_add_f32_e32 v90, 1.0, v89
	v_log_f32_e32 v90, v90
	s_nop 0
	v_mul_f32_e32 v90, 0x3f317218, v90
	v_pk_add_f32 v[68:69], v[68:69], v[90:91] neg_lo:[0,1] neg_hi:[0,1]
	v_mul_f32_e64 v90, |v71|, s35
	v_exp_f32_e32 v119, v90
	v_min_f32_e32 v71, 0, v71
	v_pk_mul_f32 v[68:69], v[68:69], s[44:45] op_sel_hi:[1,0]
	v_add_f32_e32 v81, 1.0, v119
	v_log_f32_e32 v81, v81
	s_nop 0
	v_mul_f32_e32 v81, 0x3f317218, v81
	v_add_f32_e32 v80, 1.0, v118
	v_log_f32_e32 v80, v80
	s_nop 0
	v_mul_f32_e32 v80, 0x3f317218, v80
	v_pk_add_f32 v[70:71], v[70:71], v[80:81] neg_lo:[0,1] neg_hi:[0,1]
	v_mov_b32_e32 v67, 0
	v_pk_mul_f32 v[70:71], v[70:71], s[44:45] op_sel_hi:[1,0]
	global_store_dwordx4 v[82:83], v[68:71], off offset:448
	s_nop 1
	v_mov_b32_e32 v68, 0
	v_mov_b32_e32 v69, 0
	s_and_saveexec_b64 s[72:73], s[4:5]
	ds_read_b128 v[66:69], v72 offset:512
	s_or_b64 exec, exec, s[72:73]
	s_waitcnt lgkmcnt(0)
	v_mfma_f32_16x16x32_bf16 v[80:83], v[6:9], v[66:69], 0
	v_lshl_add_u64 v[70:71], v[78:79], 0, s[62:63]
	s_nop 6
	v_add_f32_e32 v80, v10, v80
	v_mul_f32_e64 v89, |v80|, s35
	v_exp_f32_e32 v89, v89
	v_add_f32_e32 v91, v11, v81
	v_min_f32_e32 v90, 0, v80
	v_mul_f32_e64 v80, |v91|, s35
	v_exp_f32_e32 v118, v80
	v_add_f32_e32 v82, v12, v82
	v_min_f32_e32 v91, 0, v91
	v_add_f32_e32 v83, v13, v83
	v_mul_f32_e64 v94, |v82|, s35
	v_exp_f32_e32 v120, v94
	v_min_f32_e32 v82, 0, v82
	v_add_f32_e32 v93, 1.0, v118
	v_log_f32_e32 v93, v93
	s_nop 0
	v_mul_f32_e32 v93, 0x3f317218, v93
	v_add_f32_e32 v92, 1.0, v89
	v_log_f32_e32 v92, v92
	s_nop 0
	v_mul_f32_e32 v92, 0x3f317218, v92
	v_pk_add_f32 v[90:91], v[90:91], v[92:93] neg_lo:[0,1] neg_hi:[0,1]
	v_mul_f32_e64 v92, |v83|, s35
	v_exp_f32_e32 v121, v92
	v_min_f32_e32 v83, 0, v83
	v_pk_mul_f32 v[90:91], v[90:91], s[44:45] op_sel_hi:[1,0]
	v_mfma_f32_16x16x32_bf16 v[94:97], v[2:5], v[66:69], 0
	v_add_f32_e32 v93, 1.0, v121
	v_log_f32_e32 v93, v93
	s_nop 0
	v_mul_f32_e32 v93, 0x3f317218, v93
	v_add_f32_e32 v92, 1.0, v120
	v_log_f32_e32 v92, v92
	s_nop 0
	v_mul_f32_e32 v92, 0x3f317218, v92
	v_pk_add_f32 v[82:83], v[82:83], v[92:93] neg_lo:[0,1] neg_hi:[0,1]
	v_add_f32_e32 v89, v14, v94
	v_pk_mul_f32 v[92:93], v[82:83], s[44:45] op_sel_hi:[1,0]
	v_mul_f32_e64 v82, |v89|, s35
	v_exp_f32_e32 v120, v82
	v_lshl_add_u64 v[82:83], s[2:3], 2, v[70:71]
	global_store_dwordx4 v[82:83], v[90:93], off
	v_min_f32_e32 v82, 0, v89
	v_add_f32_e32 v83, v15, v95
	v_mul_f32_e64 v90, |v83|, s35
	v_exp_f32_e32 v121, v90
	v_min_f32_e32 v83, 0, v83
	v_add_f32_e32 v92, v16, v96
	v_add_f32_e32 v91, 1.0, v121
	v_log_f32_e32 v91, v91
	s_nop 0
	v_mul_f32_e32 v91, 0x3f317218, v91
	v_mul_f32_e64 v90, |v92|, s35
	v_exp_f32_e32 v121, v90
	v_add_f32_e32 v90, 1.0, v120
	v_log_f32_e32 v90, v90
	s_nop 0
	v_mul_f32_e32 v90, 0x3f317218, v90
	v_pk_add_f32 v[82:83], v[82:83], v[90:91] neg_lo:[0,1] neg_hi:[0,1]
	v_min_f32_e32 v90, 0, v92
	v_add_f32_e32 v91, v17, v97
	v_mul_f32_e64 v92, |v91|, s35
	v_exp_f32_e32 v120, v92
	v_min_f32_e32 v91, 0, v91
	v_mfma_f32_16x16x32_bf16 v[94:97], v[22:25], v[66:69], 0
	v_add_f32_e32 v93, 1.0, v120
	v_log_f32_e32 v93, v93
	s_nop 0
	v_mul_f32_e32 v93, 0x3f317218, v93
	v_add_f32_e32 v92, 1.0, v121
	v_log_f32_e32 v92, v92
	s_nop 0
	v_mul_f32_e32 v92, 0x3f317218, v92
	v_pk_add_f32 v[90:91], v[90:91], v[92:93] neg_lo:[0,1] neg_hi:[0,1]
	v_add_f32_e32 v89, v26, v94
	v_pk_mul_f32 v[92:93], v[90:91], s[44:45] op_sel_hi:[1,0]
	v_pk_mul_f32 v[90:91], v[82:83], s[44:45] op_sel_hi:[1,0]
	v_mul_f32_e64 v82, |v89|, s35
	v_exp_f32_e32 v120, v82
	v_lshl_add_u64 v[82:83], s[10:11], 2, v[70:71]
	global_store_dwordx4 v[82:83], v[90:93], off
	v_min_f32_e32 v82, 0, v89
	v_add_f32_e32 v83, v27, v95
	v_mul_f32_e64 v90, |v83|, s35
	v_exp_f32_e32 v121, v90
	v_min_f32_e32 v83, 0, v83
	v_add_f32_e32 v92, v28, v96
	v_add_f32_e32 v91, 1.0, v121
	v_log_f32_e32 v91, v91
	s_nop 0
	v_mul_f32_e32 v91, 0x3f317218, v91
	v_mul_f32_e64 v90, |v92|, s35
	v_exp_f32_e32 v121, v90
	v_add_f32_e32 v90, 1.0, v120
	v_log_f32_e32 v90, v90
	s_nop 0
	v_mul_f32_e32 v90, 0x3f317218, v90
	v_pk_add_f32 v[82:83], v[82:83], v[90:91] neg_lo:[0,1] neg_hi:[0,1]
	v_min_f32_e32 v90, 0, v92
	v_add_f32_e32 v91, v29, v97
	v_mul_f32_e64 v92, |v91|, s35
	v_exp_f32_e32 v120, v92
	v_min_f32_e32 v91, 0, v91
	v_mfma_f32_16x16x32_bf16 v[94:97], v[18:21], v[66:69], 0
	v_add_f32_e32 v93, 1.0, v120
	v_log_f32_e32 v93, v93
	s_nop 0
	v_mul_f32_e32 v93, 0x3f317218, v93
	v_add_f32_e32 v92, 1.0, v121
	v_log_f32_e32 v92, v92
	s_nop 0
	v_mul_f32_e32 v92, 0x3f317218, v92
	v_pk_add_f32 v[90:91], v[90:91], v[92:93] neg_lo:[0,1] neg_hi:[0,1]
	v_add_f32_e32 v89, v30, v94
	v_pk_mul_f32 v[92:93], v[90:91], s[44:45] op_sel_hi:[1,0]
	v_pk_mul_f32 v[90:91], v[82:83], s[44:45] op_sel_hi:[1,0]
	v_mul_f32_e64 v82, |v89|, s35
	v_exp_f32_e32 v120, v82
	v_lshl_add_u64 v[82:83], s[12:13], 2, v[70:71]
	global_store_dwordx4 v[82:83], v[90:93], off
	v_min_f32_e32 v82, 0, v89
	v_add_f32_e32 v83, v31, v95
	v_mul_f32_e64 v90, |v83|, s35
	v_exp_f32_e32 v121, v90
	v_min_f32_e32 v83, 0, v83
	v_add_f32_e32 v92, v32, v96
	v_add_f32_e32 v91, 1.0, v121
	v_log_f32_e32 v91, v91
	s_nop 0
	v_mul_f32_e32 v91, 0x3f317218, v91
	v_mul_f32_e64 v90, |v92|, s35
	v_exp_f32_e32 v121, v90
	v_add_f32_e32 v90, 1.0, v120
	v_log_f32_e32 v90, v90
	s_nop 0
	v_mul_f32_e32 v90, 0x3f317218, v90
	v_pk_add_f32 v[82:83], v[82:83], v[90:91] neg_lo:[0,1] neg_hi:[0,1]
	v_min_f32_e32 v90, 0, v92
	v_add_f32_e32 v91, v33, v97
	v_mul_f32_e64 v92, |v91|, s35
	v_exp_f32_e32 v120, v92
	v_min_f32_e32 v91, 0, v91
	v_mfma_f32_16x16x32_bf16 v[94:97], v[38:41], v[66:69], 0
	v_add_f32_e32 v93, 1.0, v120
	v_log_f32_e32 v93, v93
	s_nop 0
	v_mul_f32_e32 v93, 0x3f317218, v93
	v_add_f32_e32 v92, 1.0, v121
	v_log_f32_e32 v92, v92
	s_nop 0
	v_mul_f32_e32 v92, 0x3f317218, v92
	v_pk_add_f32 v[90:91], v[90:91], v[92:93] neg_lo:[0,1] neg_hi:[0,1]
	v_add_f32_e32 v89, v42, v94
	v_pk_mul_f32 v[92:93], v[90:91], s[44:45] op_sel_hi:[1,0]
	v_pk_mul_f32 v[90:91], v[82:83], s[44:45] op_sel_hi:[1,0]
	v_mul_f32_e64 v82, |v89|, s35
	v_exp_f32_e32 v120, v82
	v_lshl_add_u64 v[82:83], s[14:15], 2, v[70:71]
	global_store_dwordx4 v[82:83], v[90:93], off
	v_min_f32_e32 v82, 0, v89
	v_add_f32_e32 v83, v43, v95
	v_mul_f32_e64 v90, |v83|, s35
	v_exp_f32_e32 v121, v90
	v_min_f32_e32 v83, 0, v83
	v_add_f32_e32 v92, v44, v96
	v_add_f32_e32 v91, 1.0, v121
	v_log_f32_e32 v91, v91
	s_nop 0
	v_mul_f32_e32 v91, 0x3f317218, v91
	v_mul_f32_e64 v90, |v92|, s35
	v_exp_f32_e32 v121, v90
	v_add_f32_e32 v90, 1.0, v120
	v_log_f32_e32 v90, v90
	s_nop 0
	v_mul_f32_e32 v90, 0x3f317218, v90
	v_pk_add_f32 v[82:83], v[82:83], v[90:91] neg_lo:[0,1] neg_hi:[0,1]
	v_min_f32_e32 v90, 0, v92
	v_add_f32_e32 v91, v45, v97
	v_mul_f32_e64 v92, |v91|, s35
	v_exp_f32_e32 v120, v92
	v_min_f32_e32 v91, 0, v91
	v_mfma_f32_16x16x32_bf16 v[94:97], v[34:37], v[66:69], 0
	v_add_f32_e32 v93, 1.0, v120
	v_log_f32_e32 v93, v93
	s_nop 0
	v_mul_f32_e32 v93, 0x3f317218, v93
	v_add_f32_e32 v92, 1.0, v121
	v_log_f32_e32 v92, v92
	s_nop 0
	v_mul_f32_e32 v92, 0x3f317218, v92
	v_pk_add_f32 v[90:91], v[90:91], v[92:93] neg_lo:[0,1] neg_hi:[0,1]
	v_add_f32_e32 v89, v46, v94
	v_pk_mul_f32 v[92:93], v[90:91], s[44:45] op_sel_hi:[1,0]
	v_pk_mul_f32 v[90:91], v[82:83], s[44:45] op_sel_hi:[1,0]
	v_mul_f32_e64 v82, |v89|, s35
	v_exp_f32_e32 v120, v82
	v_lshl_add_u64 v[82:83], s[16:17], 2, v[70:71]
	global_store_dwordx4 v[82:83], v[90:93], off
	v_min_f32_e32 v82, 0, v89
	v_add_f32_e32 v83, v47, v95
	v_mul_f32_e64 v90, |v83|, s35
	v_exp_f32_e32 v121, v90
	v_min_f32_e32 v83, 0, v83
	v_add_f32_e32 v92, v48, v96
	v_add_f32_e32 v91, 1.0, v121
	v_log_f32_e32 v91, v91
	s_nop 0
	v_mul_f32_e32 v91, 0x3f317218, v91
	v_mul_f32_e64 v90, |v92|, s35
	v_exp_f32_e32 v121, v90
	v_add_f32_e32 v90, 1.0, v120
	v_log_f32_e32 v90, v90
	s_nop 0
	v_mul_f32_e32 v90, 0x3f317218, v90
	v_pk_add_f32 v[82:83], v[82:83], v[90:91] neg_lo:[0,1] neg_hi:[0,1]
	v_min_f32_e32 v90, 0, v92
	v_add_f32_e32 v91, v49, v97
	v_mul_f32_e64 v92, |v91|, s35
	v_exp_f32_e32 v120, v92
	v_min_f32_e32 v91, 0, v91
	v_mfma_f32_16x16x32_bf16 v[94:97], v[54:57], v[66:69], 0
	v_mfma_f32_16x16x32_bf16 v[66:69], v[50:53], v[66:69], 0
	s_nop 7
	v_add_f32_e32 v66, v62, v66
	v_add_f32_e32 v67, v63, v67
	v_add_f32_e32 v68, v64, v68
	v_add_f32_e32 v69, v65, v69
	v_add_f32_e32 v93, 1.0, v120
	v_log_f32_e32 v93, v93
	s_nop 0
	v_mul_f32_e32 v93, 0x3f317218, v93
	v_add_f32_e32 v92, 1.0, v121
	v_log_f32_e32 v92, v92
	s_nop 0
	v_mul_f32_e32 v92, 0x3f317218, v92
	v_pk_add_f32 v[90:91], v[90:91], v[92:93] neg_lo:[0,1] neg_hi:[0,1]
	v_add_f32_e32 v89, v58, v94
	v_pk_mul_f32 v[92:93], v[90:91], s[44:45] op_sel_hi:[1,0]
	v_pk_mul_f32 v[90:91], v[82:83], s[44:45] op_sel_hi:[1,0]
	v_mul_f32_e64 v82, |v89|, s35
	v_exp_f32_e32 v120, v82
	v_lshl_add_u64 v[82:83], s[18:19], 2, v[70:71]
	global_store_dwordx4 v[82:83], v[90:93], off
	v_min_f32_e32 v82, 0, v89
	v_add_f32_e32 v83, v59, v95
	v_mul_f32_e64 v90, |v83|, s35
	v_exp_f32_e32 v121, v90
	v_min_f32_e32 v83, 0, v83
	v_add_f32_e32 v92, v60, v96
	v_add_f32_e32 v91, 1.0, v121
	v_log_f32_e32 v91, v91
	s_nop 0
	v_mul_f32_e32 v91, 0x3f317218, v91
	v_mul_f32_e64 v90, |v92|, s35
	v_exp_f32_e32 v121, v90
	v_add_f32_e32 v90, 1.0, v120
	v_log_f32_e32 v90, v90
	s_nop 0
	v_mul_f32_e32 v90, 0x3f317218, v90
	v_pk_add_f32 v[82:83], v[82:83], v[90:91] neg_lo:[0,1] neg_hi:[0,1]
	v_min_f32_e32 v90, 0, v92
	v_add_f32_e32 v91, v61, v97
	v_mul_f32_e64 v92, |v91|, s35
	v_exp_f32_e32 v120, v92
	v_min_f32_e32 v91, 0, v91
	v_add_f32_e32 v93, 1.0, v120
	v_log_f32_e32 v93, v93
	s_nop 0
	v_mul_f32_e32 v93, 0x3f317218, v93
	v_add_f32_e32 v92, 1.0, v121
	v_log_f32_e32 v92, v92
	s_nop 0
	v_mul_f32_e32 v92, 0x3f317218, v92
	v_pk_add_f32 v[90:91], v[90:91], v[92:93] neg_lo:[0,1] neg_hi:[0,1]
	s_nop 0
	v_pk_mul_f32 v[92:93], v[90:91], s[44:45] op_sel_hi:[1,0]
	v_pk_mul_f32 v[90:91], v[82:83], s[44:45] op_sel_hi:[1,0]
	v_mul_f32_e64 v82, |v66|, s35
	v_exp_f32_e32 v89, v82
	v_lshl_add_u64 v[82:83], s[20:21], 2, v[70:71]
	global_store_dwordx4 v[82:83], v[90:93], off
	v_min_f32_e32 v66, 0, v66
	v_lshl_add_u64 v[70:71], s[22:23], 2, v[70:71]
	v_mul_f32_e64 v82, |v67|, s35
	v_exp_f32_e32 v116, v82
	v_min_f32_e32 v67, 0, v67
	v_mul_f32_e64 v90, |v68|, s35
	v_min_f32_e32 v68, 0, v68
	v_add_f32_e32 v83, 1.0, v116
	v_log_f32_e32 v83, v83
	s_nop 0
	v_mul_f32_e32 v83, 0x3f317218, v83
	v_exp_f32_e32 v116, v90
	v_add_f32_e32 v82, 1.0, v89
	v_log_f32_e32 v82, v82
	s_nop 0
	v_mul_f32_e32 v82, 0x3f317218, v82
	v_pk_add_f32 v[66:67], v[66:67], v[82:83] neg_lo:[0,1] neg_hi:[0,1]
	v_mul_f32_e64 v82, |v69|, s35
	v_exp_f32_e32 v117, v82
	v_min_f32_e32 v69, 0, v69
	v_pk_mul_f32 v[66:67], v[66:67], s[44:45] op_sel_hi:[1,0]
	v_add_f32_e32 v81, 1.0, v117
	v_log_f32_e32 v81, v81
	s_nop 0
	v_mul_f32_e32 v81, 0x3f317218, v81
	v_add_f32_e32 v80, 1.0, v116
	v_log_f32_e32 v80, v80
	s_nop 0
	v_mul_f32_e32 v80, 0x3f317218, v80
	v_pk_add_f32 v[68:69], v[68:69], v[80:81] neg_lo:[0,1] neg_hi:[0,1]
	s_nop 0
	v_pk_mul_f32 v[68:69], v[68:69], s[44:45] op_sel_hi:[1,0]
	global_store_dwordx4 v[70:71], v[66:69], off
	v_mov_b32_e32 v70, 0
	v_mov_b32_e32 v71, 0
	v_mov_b32_e32 v66, 0
	v_mov_b32_e32 v68, 0
	v_mov_b32_e32 v69, 0
	s_and_saveexec_b64 s[72:73], s[4:5]
	ds_read_b128 v[68:71], v72 offset:1024
	s_or_b64 exec, exec, s[72:73]
	s_waitcnt lgkmcnt(0)
	v_mfma_f32_16x16x32_bf16 v[90:93], v[6:9], v[68:71], 0
	v_lshl_add_u64 v[80:81], v[78:79], 0, s[64:65]
	s_nop 6
	v_add_f32_e32 v67, v10, v90
	v_mul_f32_e64 v82, |v67|, s35
	v_exp_f32_e32 v89, v82
	v_add_f32_e32 v91, v11, v91
	v_min_f32_e32 v90, 0, v67
	v_mul_f32_e64 v67, |v91|, s35
	v_exp_f32_e32 v67, v67
	v_min_f32_e32 v91, 0, v91
	v_add_f32_e32 v93, v13, v93
	v_add_f32_e32 v95, 1.0, v67
	v_log_f32_e32 v95, v95
	s_nop 0
	v_mul_f32_e32 v95, 0x3f317218, v95
	v_add_f32_e32 v67, v12, v92
	v_mul_f32_e64 v92, |v67|, s35
	v_exp_f32_e32 v122, v92
	v_min_f32_e32 v92, 0, v67
	v_add_f32_e32 v94, 1.0, v89
	v_log_f32_e32 v94, v94
	s_nop 0
	v_mul_f32_e32 v94, 0x3f317218, v94
	v_pk_add_f32 v[90:91], v[90:91], v[94:95] neg_lo:[0,1] neg_hi:[0,1]
	v_mul_f32_e64 v94, |v93|, s35
	v_exp_f32_e32 v123, v94
	v_min_f32_e32 v93, 0, v93
	v_pk_mul_f32 v[90:91], v[90:91], s[44:45] op_sel_hi:[1,0]
	v_lshl_add_u64 v[98:99], s[2:3], 2, v[80:81]
	v_add_f32_e32 v95, 1.0, v123
	v_log_f32_e32 v95, v95
	s_nop 0
	v_mul_f32_e32 v95, 0x3f317218, v95
	v_add_f32_e32 v94, 1.0, v122
	v_log_f32_e32 v94, v94
	s_nop 0
	v_mul_f32_e32 v94, 0x3f317218, v94
	v_pk_add_f32 v[92:93], v[92:93], v[94:95] neg_lo:[0,1] neg_hi:[0,1]
	v_mfma_f32_16x16x32_bf16 v[94:97], v[2:5], v[68:71], 0
	v_mul_f32_e64 v92, v92, s44
	v_mul_f32_e64 v93, v93, s44
	global_store_dwordx4 v[98:99], v[90:93], off
	s_nop 4
	v_add_f32_e32 v67, v14, v94
	v_mul_f32_e64 v89, |v67|, s35
	v_exp_f32_e32 v89, v89
	v_min_f32_e32 v90, 0, v67
	v_add_f32_e32 v91, v15, v95
	v_mul_f32_e64 v92, |v91|, s35
	v_exp_f32_e32 v122, v92
	v_min_f32_e32 v91, 0, v91
	v_add_f32_e32 v94, v16, v96
	v_add_f32_e32 v93, 1.0, v122
	v_log_f32_e32 v93, v93
	s_nop 0
	v_mul_f32_e32 v93, 0x3f317218, v93
	v_mul_f32_e64 v92, |v94|, s35
	v_exp_f32_e32 v122, v92
	v_add_f32_e32 v92, 1.0, v89
	v_log_f32_e32 v92, v92
	s_nop 0
	v_mul_f32_e32 v92, 0x3f317218, v92
	v_pk_add_f32 v[90:91], v[90:91], v[92:93] neg_lo:[0,1] neg_hi:[0,1]
	v_add_f32_e32 v93, v17, v97
	v_min_f32_e32 v92, 0, v94
	v_mul_f32_e64 v94, |v93|, s35
	v_exp_f32_e32 v123, v94
	v_min_f32_e32 v93, 0, v93
	v_pk_mul_f32 v[90:91], v[90:91], s[44:45] op_sel_hi:[1,0]
	v_lshl_add_u64 v[98:99], s[10:11], 2, v[80:81]
	v_add_f32_e32 v95, 1.0, v123
	v_log_f32_e32 v95, v95
	s_nop 0
	v_mul_f32_e32 v95, 0x3f317218, v95
	v_add_f32_e32 v94, 1.0, v122
	v_log_f32_e32 v94, v94
	s_nop 0
	v_mul_f32_e32 v94, 0x3f317218, v94
	v_pk_add_f32 v[92:93], v[92:93], v[94:95] neg_lo:[0,1] neg_hi:[0,1]
	v_mfma_f32_16x16x32_bf16 v[94:97], v[22:25], v[68:71], 0
	v_mul_f32_e64 v92, v92, s44
	v_mul_f32_e64 v93, v93, s44
	global_store_dwordx4 v[98:99], v[90:93], off
	s_nop 4
	v_add_f32_e32 v67, v26, v94
	v_mul_f32_e64 v89, |v67|, s35
	v_exp_f32_e32 v89, v89
	v_min_f32_e32 v90, 0, v67
	v_add_f32_e32 v91, v27, v95
	v_mul_f32_e64 v92, |v91|, s35
	v_exp_f32_e32 v122, v92
	v_min_f32_e32 v91, 0, v91
	v_add_f32_e32 v94, v28, v96
	v_add_f32_e32 v93, 1.0, v122
	v_log_f32_e32 v93, v93
	s_nop 0
	v_mul_f32_e32 v93, 0x3f317218, v93
	v_mul_f32_e64 v92, |v94|, s35
	v_exp_f32_e32 v122, v92
	v_add_f32_e32 v92, 1.0, v89
	v_log_f32_e32 v92, v92
	s_nop 0
	v_mul_f32_e32 v92, 0x3f317218, v92
	v_pk_add_f32 v[90:91], v[90:91], v[92:93] neg_lo:[0,1] neg_hi:[0,1]
	v_add_f32_e32 v93, v29, v97
	v_min_f32_e32 v92, 0, v94
	v_mul_f32_e64 v94, |v93|, s35
	v_exp_f32_e32 v123, v94
	v_min_f32_e32 v93, 0, v93
	v_pk_mul_f32 v[90:91], v[90:91], s[44:45] op_sel_hi:[1,0]
	v_lshl_add_u64 v[98:99], s[12:13], 2, v[80:81]
	v_add_f32_e32 v95, 1.0, v123
	v_log_f32_e32 v95, v95
	s_nop 0
	v_mul_f32_e32 v95, 0x3f317218, v95
	v_add_f32_e32 v94, 1.0, v122
	v_log_f32_e32 v94, v94
	s_nop 0
	v_mul_f32_e32 v94, 0x3f317218, v94
	v_pk_add_f32 v[92:93], v[92:93], v[94:95] neg_lo:[0,1] neg_hi:[0,1]
	v_mfma_f32_16x16x32_bf16 v[94:97], v[18:21], v[68:71], 0
	v_mul_f32_e64 v92, v92, s44
	v_mul_f32_e64 v93, v93, s44
	global_store_dwordx4 v[98:99], v[90:93], off
	s_nop 4
	v_add_f32_e32 v67, v30, v94
	v_mul_f32_e64 v89, |v67|, s35
	v_exp_f32_e32 v89, v89
	v_min_f32_e32 v90, 0, v67
	v_add_f32_e32 v91, v31, v95
	v_mul_f32_e64 v92, |v91|, s35
	v_exp_f32_e32 v122, v92
	v_min_f32_e32 v91, 0, v91
	v_add_f32_e32 v94, v32, v96
	v_add_f32_e32 v93, 1.0, v122
	v_log_f32_e32 v93, v93
	s_nop 0
	v_mul_f32_e32 v93, 0x3f317218, v93
	v_mul_f32_e64 v92, |v94|, s35
	v_exp_f32_e32 v122, v92
	v_add_f32_e32 v92, 1.0, v89
	v_log_f32_e32 v92, v92
	s_nop 0
	v_mul_f32_e32 v92, 0x3f317218, v92
	v_pk_add_f32 v[90:91], v[90:91], v[92:93] neg_lo:[0,1] neg_hi:[0,1]
	v_add_f32_e32 v93, v33, v97
	v_min_f32_e32 v92, 0, v94
	v_mul_f32_e64 v94, |v93|, s35
	v_exp_f32_e32 v123, v94
	v_min_f32_e32 v93, 0, v93
	v_pk_mul_f32 v[90:91], v[90:91], s[44:45] op_sel_hi:[1,0]
	v_lshl_add_u64 v[98:99], s[14:15], 2, v[80:81]
	v_add_f32_e32 v95, 1.0, v123
	v_log_f32_e32 v95, v95
	s_nop 0
	v_mul_f32_e32 v95, 0x3f317218, v95
	v_add_f32_e32 v94, 1.0, v122
	v_log_f32_e32 v94, v94
	s_nop 0
	v_mul_f32_e32 v94, 0x3f317218, v94
	v_pk_add_f32 v[92:93], v[92:93], v[94:95] neg_lo:[0,1] neg_hi:[0,1]
	v_mfma_f32_16x16x32_bf16 v[94:97], v[38:41], v[68:71], 0
	v_mul_f32_e64 v92, v92, s44
	v_mul_f32_e64 v93, v93, s44
	global_store_dwordx4 v[98:99], v[90:93], off
	s_nop 4
	v_add_f32_e32 v67, v42, v94
	v_mul_f32_e64 v89, |v67|, s35
	v_exp_f32_e32 v89, v89
	v_min_f32_e32 v90, 0, v67
	v_add_f32_e32 v91, v43, v95
	v_mul_f32_e64 v92, |v91|, s35
	v_exp_f32_e32 v122, v92
	v_min_f32_e32 v91, 0, v91
	v_add_f32_e32 v94, v44, v96
	v_add_f32_e32 v93, 1.0, v122
	v_log_f32_e32 v93, v93
	s_nop 0
	v_mul_f32_e32 v93, 0x3f317218, v93
	v_mul_f32_e64 v92, |v94|, s35
	v_exp_f32_e32 v122, v92
	v_add_f32_e32 v92, 1.0, v89
	v_log_f32_e32 v92, v92
	s_nop 0
	v_mul_f32_e32 v92, 0x3f317218, v92
	v_pk_add_f32 v[90:91], v[90:91], v[92:93] neg_lo:[0,1] neg_hi:[0,1]
	v_add_f32_e32 v93, v45, v97
	v_min_f32_e32 v92, 0, v94
	v_mul_f32_e64 v94, |v93|, s35
	v_exp_f32_e32 v123, v94
	v_min_f32_e32 v93, 0, v93
	v_pk_mul_f32 v[90:91], v[90:91], s[44:45] op_sel_hi:[1,0]
	v_lshl_add_u64 v[98:99], s[16:17], 2, v[80:81]
	v_add_f32_e32 v95, 1.0, v123
	v_log_f32_e32 v95, v95
	s_nop 0
	v_mul_f32_e32 v95, 0x3f317218, v95
	v_add_f32_e32 v94, 1.0, v122
	v_log_f32_e32 v94, v94
	s_nop 0
	v_mul_f32_e32 v94, 0x3f317218, v94
	v_pk_add_f32 v[92:93], v[92:93], v[94:95] neg_lo:[0,1] neg_hi:[0,1]
	v_mfma_f32_16x16x32_bf16 v[94:97], v[34:37], v[68:71], 0
	v_mul_f32_e64 v92, v92, s44
	v_mul_f32_e64 v93, v93, s44
	global_store_dwordx4 v[98:99], v[90:93], off
	s_nop 4
	v_add_f32_e32 v67, v46, v94
	v_mul_f32_e64 v89, |v67|, s35
	v_exp_f32_e32 v89, v89
	v_min_f32_e32 v90, 0, v67
	v_add_f32_e32 v91, v47, v95
	v_mul_f32_e64 v92, |v91|, s35
	v_exp_f32_e32 v122, v92
	v_min_f32_e32 v91, 0, v91
	v_add_f32_e32 v94, v48, v96
	v_add_f32_e32 v93, 1.0, v122
	v_log_f32_e32 v93, v93
	s_nop 0
	v_mul_f32_e32 v93, 0x3f317218, v93
	v_mul_f32_e64 v92, |v94|, s35
	v_exp_f32_e32 v122, v92
	v_add_f32_e32 v92, 1.0, v89
	v_log_f32_e32 v92, v92
	s_nop 0
	v_mul_f32_e32 v92, 0x3f317218, v92
	v_pk_add_f32 v[90:91], v[90:91], v[92:93] neg_lo:[0,1] neg_hi:[0,1]
	v_add_f32_e32 v93, v49, v97
	v_min_f32_e32 v92, 0, v94
	v_mul_f32_e64 v94, |v93|, s35
	v_exp_f32_e32 v123, v94
	v_min_f32_e32 v93, 0, v93
	v_pk_mul_f32 v[90:91], v[90:91], s[44:45] op_sel_hi:[1,0]
	v_lshl_add_u64 v[98:99], s[18:19], 2, v[80:81]
	v_add_f32_e32 v95, 1.0, v123
	v_log_f32_e32 v95, v95
	s_nop 0
	v_mul_f32_e32 v95, 0x3f317218, v95
	v_add_f32_e32 v94, 1.0, v122
	v_log_f32_e32 v94, v94
	s_nop 0
	v_mul_f32_e32 v94, 0x3f317218, v94
	v_pk_add_f32 v[92:93], v[92:93], v[94:95] neg_lo:[0,1] neg_hi:[0,1]
	v_mfma_f32_16x16x32_bf16 v[94:97], v[54:57], v[68:71], 0
	v_mul_f32_e64 v92, v92, s44
	v_mul_f32_e64 v93, v93, s44
	global_store_dwordx4 v[98:99], v[90:93], off
	v_mfma_f32_16x16x32_bf16 v[68:71], v[50:53], v[68:71], 0
	s_nop 3
	v_add_f32_e32 v67, v58, v94
	v_mul_f32_e64 v89, |v67|, s35
	v_exp_f32_e32 v89, v89
	v_min_f32_e32 v90, 0, v67
	v_add_f32_e32 v69, v63, v69
	v_add_f32_e32 v70, v64, v70
	v_add_f32_e32 v91, v59, v95
	v_mul_f32_e64 v92, |v91|, s35
	v_exp_f32_e32 v122, v92
	v_min_f32_e32 v91, 0, v91
	v_add_f32_e32 v71, v65, v71
	v_add_f32_e32 v94, v60, v96
	v_add_f32_e32 v93, 1.0, v122
	v_log_f32_e32 v93, v93
	s_nop 0
	v_mul_f32_e32 v93, 0x3f317218, v93
	v_mul_f32_e64 v92, |v94|, s35
	v_exp_f32_e32 v122, v92
	v_add_f32_e32 v92, 1.0, v89
	v_log_f32_e32 v92, v92
	s_nop 0
	v_mul_f32_e32 v92, 0x3f317218, v92
	v_pk_add_f32 v[90:91], v[90:91], v[92:93] neg_lo:[0,1] neg_hi:[0,1]
	v_add_f32_e32 v93, v61, v97
	v_min_f32_e32 v92, 0, v94
	v_mul_f32_e64 v94, |v93|, s35
	v_exp_f32_e32 v123, v94
	v_min_f32_e32 v93, 0, v93
	v_pk_mul_f32 v[90:91], v[90:91], s[44:45] op_sel_hi:[1,0]
	v_add_f32_e32 v95, 1.0, v123
	v_log_f32_e32 v95, v95
	s_nop 0
	v_mul_f32_e32 v95, 0x3f317218, v95
	v_add_f32_e32 v94, 1.0, v122
	v_log_f32_e32 v94, v94
	s_nop 0
	v_mul_f32_e32 v94, 0x3f317218, v94
	v_add_f32_e32 v67, v62, v68
	v_mul_f32_e64 v68, |v67|, s35
	v_exp_f32_e32 v89, v68
	v_pk_add_f32 v[92:93], v[92:93], v[94:95] neg_lo:[0,1] neg_hi:[0,1]
	v_lshl_add_u64 v[94:95], s[20:21], 2, v[80:81]
	v_pk_mul_f32 v[92:93], v[92:93], s[44:45] op_sel_hi:[1,0]
	v_min_f32_e32 v68, 0, v67
	global_store_dwordx4 v[94:95], v[90:93], off
	v_lshl_add_u64 v[80:81], s[22:23], 2, v[80:81]
	s_nop 0
	v_mul_f32_e64 v90, |v69|, s35
	v_exp_f32_e32 v118, v90
	v_min_f32_e32 v69, 0, v69
	v_add_f32_e32 v91, 1.0, v118
	v_log_f32_e32 v91, v91
	s_nop 0
	v_mul_f32_e32 v91, 0x3f317218, v91
	v_mul_f32_e64 v90, |v70|, s35
	v_exp_f32_e32 v118, v90
	v_min_f32_e32 v70, 0, v70
	v_add_f32_e32 v90, 1.0, v89
	v_log_f32_e32 v90, v90
	s_nop 0
	v_mul_f32_e32 v90, 0x3f317218, v90
	v_pk_add_f32 v[68:69], v[68:69], v[90:91] neg_lo:[0,1] neg_hi:[0,1]
	v_mul_f32_e64 v90, |v71|, s35
	v_exp_f32_e32 v119, v90
	v_min_f32_e32 v71, 0, v71
	v_pk_mul_f32 v[68:69], v[68:69], s[44:45] op_sel_hi:[1,0]
	v_add_f32_e32 v83, 1.0, v119
	v_log_f32_e32 v83, v83
	s_nop 0
	v_mul_f32_e32 v83, 0x3f317218, v83
	v_cmp_lt_f32_e64 vcc, |v118|, s45
	v_add_f32_e32 v82, 1.0, v118
	v_log_f32_e32 v82, v82
	s_nop 0
	v_mul_f32_e32 v82, 0x3f317218, v82
	v_pk_add_f32 v[70:71], v[70:71], v[82:83] neg_lo:[0,1] neg_hi:[0,1]
	v_mov_b32_e32 v67, 0
	v_pk_mul_f32 v[70:71], v[70:71], s[44:45] op_sel_hi:[1,0]
	global_store_dwordx4 v[80:81], v[68:71], off
	s_nop 1
	v_mov_b32_e32 v68, 0
	v_mov_b32_e32 v69, 0
	s_and_saveexec_b64 s[72:73], s[4:5]
	s_cbranch_execz .LBB0_146
	ds_read_b128 v[66:69], v72 offset:1536
	s_branch .LBB0_146
